# baseline (speedup 1.0000x reference)
.Lq2_nd1_2:
	s_nop 3
	s_waitcnt vmcnt(6)
	v_mfma_scale_f32_32x32x64_f8f6f4 v[2:17], v[34:41], v[146:153], 0, v203, v203 op_sel_hi:[0,0,0]
	v_exp_f32_e64 v18, -v18
	v_exp_f32_e64 v19, -v19
	v_exp_f32_e64 v20, -v20
	v_exp_f32_e64 v21, -v21
	v_add_co_u32_e64 v200, s[42:43], v200, v200
	v_add_co_u32_e64 v200, s[48:49], v200, v200
	v_add_co_u32_e64 v200, s[50:51], v200, v200
	v_add_co_u32_e64 v200, s[56:57], v200, v200
	v_pk_add_f32 v[18:19], v[18:19], v[178:179]
	v_pk_add_f32 v[20:21], v[20:21], v[180:181]
	s_mov_b64 exec, s[42:43]
	v_mul_f32_e32 v220, v220, v18
	s_mov_b64 exec, s[48:49]
	v_mul_f32_e32 v221, v221, v19
	s_mov_b64 exec, s[50:51]
	v_mul_f32_e32 v222, v222, v20
	s_mov_b64 exec, s[56:57]
	v_mul_f32_e32 v223, v223, v21
	s_mov_b64 exec, -1
	s_nop 1
	s_waitcnt vmcnt(4)
	v_mfma_scale_f32_32x32x64_f8f6f4 v[2:17], v[42:49], v[154:161], v[2:17], v203, v203 op_sel_hi:[0,0,0]
	v_exp_f32_e64 v22, -v22
	v_exp_f32_e64 v23, -v23
	v_exp_f32_e64 v24, -v24
	v_exp_f32_e64 v25, -v25
	v_add_co_u32_e64 v200, s[42:43], v200, v200
	v_add_co_u32_e64 v200, s[48:49], v200, v200
	v_add_co_u32_e64 v200, s[50:51], v200, v200
	v_add_co_u32_e64 v200, s[56:57], v200, v200
	v_pk_add_f32 v[22:23], v[22:23], v[182:183]
	v_pk_add_f32 v[24:25], v[24:25], v[184:185]
	s_mov_b64 exec, s[42:43]
	v_mul_f32_e32 v224, v224, v22
	s_mov_b64 exec, s[48:49]
	v_mul_f32_e32 v225, v225, v23
	s_mov_b64 exec, s[50:51]
	v_mul_f32_e32 v226, v226, v24
	s_mov_b64 exec, s[56:57]
	v_mul_f32_e32 v227, v227, v25
	s_mov_b64 exec, -1
	s_nop 1
	s_waitcnt vmcnt(2)
	v_mfma_scale_f32_32x32x64_f8f6f4 v[2:17], v[50:57], v[138:145], v[2:17], v203, v203 op_sel_hi:[0,0,0]
	v_exp_f32_e64 v26, -v26
	v_exp_f32_e64 v27, -v27
	v_exp_f32_e64 v28, -v28
	v_exp_f32_e64 v29, -v29
	v_add_co_u32_e64 v200, s[42:43], v200, v200
	v_add_co_u32_e64 v200, s[48:49], v200, v200
	v_add_co_u32_e64 v200, s[50:51], v200, v200
	v_add_co_u32_e64 v200, s[56:57], v200, v200
	v_pk_add_f32 v[26:27], v[26:27], v[186:187]
	v_pk_add_f32 v[28:29], v[28:29], v[188:189]
	s_mov_b64 exec, s[42:43]
	v_mul_f32_e32 v228, v228, v26
	s_mov_b64 exec, s[48:49]
	v_mul_f32_e32 v229, v229, v27
	s_mov_b64 exec, s[50:51]
	v_mul_f32_e32 v230, v230, v28
	s_mov_b64 exec, s[56:57]
	v_mul_f32_e32 v231, v231, v29
	s_mov_b64 exec, -1
	s_nop 1
	s_waitcnt vmcnt(0)
	v_mfma_scale_f32_32x32x64_f8f6f4 v[2:17], v[58:65], v[130:137], v[2:17], v203, v203 op_sel_hi:[0,0,0]
	v_exp_f32_e64 v30, -v30
	v_exp_f32_e64 v31, -v31
	v_exp_f32_e64 v32, -v32
	v_exp_f32_e64 v33, -v33
	v_add_co_u32_e64 v200, s[42:43], v200, v200
	v_add_co_u32_e64 v200, s[48:49], v200, v200
	v_add_co_u32_e64 v200, s[50:51], v200, v200
	v_add_co_u32_e64 v200, s[56:57], v200, v200
	v_pk_add_f32 v[30:31], v[30:31], v[190:191]
	v_pk_add_f32 v[32:33], v[32:33], v[192:193]
	s_mov_b64 exec, s[42:43]
	v_mul_f32_e32 v232, v232, v30
	s_mov_b64 exec, s[48:49]
	v_mul_f32_e32 v233, v233, v31
	s_mov_b64 exec, s[50:51]
	v_mul_f32_e32 v234, v234, v32
	s_mov_b64 exec, s[56:57]
	v_mul_f32_e32 v235, v235, v33
	s_mov_b64 exec, -1
	s_nop 1
	s_lshl_b32 s34, s39, 2
	s_add_i32 s34, s34, 3
	s_add_i32 s34, s34, s35
	s_and_b32 s41, s34, 15
	s_add_i32 s54, s34, 1
	s_and_b32 s54, s54, 15
	s_lshl_b32 s55, s41, 8
	s_lshl_b32 s38, s52, 12
	s_add_i32 s55, s55, s38
	v_lshl_add_u32 v236, v194, 2, s55
	ds_read_b32 v200, v236
	s_cmp_eq_u32 s39, 3
	s_cbranch_scc1 .Lq2_nobl
	s_lshl_b32 s34, s54, 3
	s_add_i32 s34, s34, s52
	s_lshl_b32 s34, s34, 13
	s_add_i32 s34, s34, s53
	buffer_load_dwordx4 v[106:109], v195, s[44:47], s34 offen
	s_or_b32 s42, s34, 0x400
	buffer_load_dwordx4 v[110:113], v195, s[44:47], s42 offen
	s_or_b32 s43, s34, 0x800
	buffer_load_dwordx4 v[122:125], v195, s[44:47], s43 offen
	s_or_b32 s42, s34, 0xc00
	buffer_load_dwordx4 v[126:129], v195, s[44:47], s42 offen
	s_or_b32 s43, s34, 0x1000
	buffer_load_dwordx4 v[114:117], v195, s[44:47], s43 offen
	s_or_b32 s42, s34, 0x1400
	buffer_load_dwordx4 v[118:121], v195, s[44:47], s42 offen
	s_or_b32 s43, s34, 0x1800
	buffer_load_dwordx4 v[98:101], v195, s[44:47], s43 offen
	s_or_b32 s42, s34, 0x1c00
	buffer_load_dwordx4 v[102:105], v195, s[44:47], s42 offen
.Lq2_nobl:
	s_lshl_b32 s55, s41, 3
	s_add_i32 s55, s55, s52
	s_cmp_lg_u32 s55, s33
	s_cbranch_scc1 .Lq2_nd0_3
	v_cndmask_b32_e64 v2, v2, v198, s[0:1]
	v_cndmask_b32_e64 v3, v3, v198, s[2:3]
	v_cndmask_b32_e64 v4, v4, v198, s[4:5]
	v_cndmask_b32_e64 v5, v5, v198, s[6:7]
	v_cndmask_b32_e64 v6, v6, v198, s[8:9]
	v_cndmask_b32_e64 v7, v7, v198, s[10:11]
	v_cndmask_b32_e64 v8, v8, v198, s[12:13]
	v_cndmask_b32_e64 v9, v9, v198, s[14:15]
	v_cndmask_b32_e64 v10, v10, v198, s[16:17]
	v_cndmask_b32_e64 v11, v11, v198, s[18:19]
	v_cndmask_b32_e64 v12, v12, v198, s[20:21]
	v_cndmask_b32_e64 v13, v13, v198, s[22:23]
	v_cndmask_b32_e64 v14, v14, v198, s[24:25]
	v_cndmask_b32_e64 v15, v15, v198, s[26:27]
	v_cndmask_b32_e64 v16, v16, v198, s[28:29]
	v_cndmask_b32_e64 v17, v17, v198, s[30:31]

.Lq2_nd1_3:
	s_nop 3
	s_cmp_eq_u32 s39, 3
	s_cbranch_scc1 .Lq2_lasthalf
	s_waitcnt vmcnt(6)
	v_mfma_scale_f32_32x32x64_f8f6f4 v[2:17], v[34:41], v[106:113], 0, v203, v203 op_sel_hi:[0,0,0]
	ds_read_b128 v[236:239], v202 offset:64
	v_exp_f32_e64 v18, -v18
	v_exp_f32_e64 v19, -v19
	v_exp_f32_e64 v20, -v20
	v_exp_f32_e64 v21, -v21
	v_add_co_u32_e64 v200, s[42:43], v200, v200
	v_add_co_u32_e64 v200, s[48:49], v200, v200
	v_add_co_u32_e64 v200, s[50:51], v200, v200
	v_add_co_u32_e64 v200, s[56:57], v200, v200
	v_pk_add_f32 v[18:19], v[18:19], v[178:179]
	v_pk_add_f32 v[20:21], v[20:21], v[180:181]
	s_mov_b64 exec, s[42:43]
	v_mul_f32_e32 v220, v220, v18
	s_mov_b64 exec, s[48:49]
	v_mul_f32_e32 v221, v221, v19
	s_mov_b64 exec, s[50:51]
	v_mul_f32_e32 v222, v222, v20
	s_mov_b64 exec, s[56:57]
	v_mul_f32_e32 v223, v223, v21
	s_mov_b64 exec, -1
	s_nop 1
	v_log_f32_e32 v18, v220
	v_log_f32_e32 v19, v221
	v_log_f32_e32 v20, v222
	v_log_f32_e32 v21, v223
	s_waitcnt lgkmcnt(0)
	v_pk_fma_f32 v[0:1], v[18:19], v[236:237], v[0:1]
	v_pk_fma_f32 v[0:1], v[20:21], v[238:239], v[0:1]
	s_waitcnt vmcnt(4)
	v_mfma_scale_f32_32x32x64_f8f6f4 v[2:17], v[42:49], v[122:129], v[2:17], v203, v203 op_sel_hi:[0,0,0]
	ds_read_b128 v[236:239], v202 offset:80
	v_exp_f32_e64 v22, -v22
	v_exp_f32_e64 v23, -v23
	v_exp_f32_e64 v24, -v24
	v_exp_f32_e64 v25, -v25
	v_add_co_u32_e64 v200, s[42:43], v200, v200
	v_add_co_u32_e64 v200, s[48:49], v200, v200
	v_add_co_u32_e64 v200, s[50:51], v200, v200
	v_add_co_u32_e64 v200, s[56:57], v200, v200
	v_pk_add_f32 v[22:23], v[22:23], v[182:183]
	v_pk_add_f32 v[24:25], v[24:25], v[184:185]
	s_mov_b64 exec, s[42:43]
	v_mul_f32_e32 v224, v224, v22
	s_mov_b64 exec, s[48:49]
	v_mul_f32_e32 v225, v225, v23
	s_mov_b64 exec, s[50:51]
	v_mul_f32_e32 v226, v226, v24
	s_mov_b64 exec, s[56:57]
	v_mul_f32_e32 v227, v227, v25
	s_mov_b64 exec, -1
	s_nop 1
	v_log_f32_e32 v22, v224
	v_log_f32_e32 v23, v225
	v_log_f32_e32 v24, v226
	v_log_f32_e32 v25, v227
	s_waitcnt lgkmcnt(0)
	v_pk_fma_f32 v[0:1], v[22:23], v[236:237], v[0:1]
	v_pk_fma_f32 v[0:1], v[24:25], v[238:239], v[0:1]
	s_waitcnt vmcnt(2)
	v_mfma_scale_f32_32x32x64_f8f6f4 v[2:17], v[50:57], v[114:121], v[2:17], v203, v203 op_sel_hi:[0,0,0]
	ds_read_b128 v[236:239], v202 offset:96
	v_exp_f32_e64 v26, -v26
	v_exp_f32_e64 v27, -v27
	v_exp_f32_e64 v28, -v28
	v_exp_f32_e64 v29, -v29
	v_add_co_u32_e64 v200, s[42:43], v200, v200
	v_add_co_u32_e64 v200, s[48:49], v200, v200
	v_add_co_u32_e64 v200, s[50:51], v200, v200
	v_add_co_u32_e64 v200, s[56:57], v200, v200
	v_pk_add_f32 v[26:27], v[26:27], v[186:187]
	v_pk_add_f32 v[28:29], v[28:29], v[188:189]
	s_mov_b64 exec, s[42:43]
	v_mul_f32_e32 v228, v228, v26
	s_mov_b64 exec, s[48:49]
	v_mul_f32_e32 v229, v229, v27
	s_mov_b64 exec, s[50:51]
	v_mul_f32_e32 v230, v230, v28
	s_mov_b64 exec, s[56:57]
	v_mul_f32_e32 v231, v231, v29
	s_mov_b64 exec, -1
	s_nop 1
	v_log_f32_e32 v26, v228
	v_log_f32_e32 v27, v229
	v_log_f32_e32 v28, v230
	v_log_f32_e32 v29, v231
	s_waitcnt lgkmcnt(0)
	v_pk_fma_f32 v[0:1], v[26:27], v[236:237], v[0:1]
	v_pk_fma_f32 v[0:1], v[28:29], v[238:239], v[0:1]
	s_waitcnt vmcnt(0)
	v_mfma_scale_f32_32x32x64_f8f6f4 v[2:17], v[58:65], v[98:105], v[2:17], v203, v203 op_sel_hi:[0,0,0]
	ds_read_b128 v[236:239], v202 offset:112
	v_exp_f32_e64 v30, -v30
	v_exp_f32_e64 v31, -v31
	v_exp_f32_e64 v32, -v32
	v_exp_f32_e64 v33, -v33
	v_add_co_u32_e64 v200, s[42:43], v200, v200
	v_add_co_u32_e64 v200, s[48:49], v200, v200
	v_add_co_u32_e64 v200, s[50:51], v200, v200
	v_add_co_u32_e64 v200, s[56:57], v200, v200
	v_pk_add_f32 v[30:31], v[30:31], v[190:191]
	v_pk_add_f32 v[32:33], v[32:33], v[192:193]
	s_mov_b64 exec, s[42:43]
	v_mul_f32_e32 v232, v232, v30
	s_mov_b64 exec, s[48:49]
	v_mul_f32_e32 v233, v233, v31
	s_mov_b64 exec, s[50:51]
	v_mul_f32_e32 v234, v234, v32
	s_mov_b64 exec, s[56:57]
	v_mul_f32_e32 v235, v235, v33
	s_mov_b64 exec, -1
	s_nop 1
	v_log_f32_e32 v30, v232
	v_log_f32_e32 v31, v233
	v_log_f32_e32 v32, v234
	v_log_f32_e32 v33, v235
	s_waitcnt lgkmcnt(0)
	v_pk_fma_f32 v[0:1], v[30:31], v[236:237], v[0:1]
	v_pk_fma_f32 v[0:1], v[32:33], v[238:239], v[0:1]
	s_branch .Lq2_halfdone
.Lq2_lasthalf:
	s_nop 3
	ds_read_b128 v[236:239], v202 offset:64
	v_exp_f32_e64 v18, -v18
	v_exp_f32_e64 v19, -v19
	v_exp_f32_e64 v20, -v20
	v_exp_f32_e64 v21, -v21
	v_add_co_u32_e64 v200, s[42:43], v200, v200
	v_add_co_u32_e64 v200, s[48:49], v200, v200
	v_add_co_u32_e64 v200, s[50:51], v200, v200
	v_add_co_u32_e64 v200, s[56:57], v200, v200
	v_pk_add_f32 v[18:19], v[18:19], v[178:179]
	v_pk_add_f32 v[20:21], v[20:21], v[180:181]
	s_mov_b64 exec, s[42:43]
	v_mul_f32_e32 v220, v220, v18
	s_mov_b64 exec, s[48:49]
	v_mul_f32_e32 v221, v221, v19
	s_mov_b64 exec, s[50:51]
	v_mul_f32_e32 v222, v222, v20
	s_mov_b64 exec, s[56:57]
	v_mul_f32_e32 v223, v223, v21
	s_mov_b64 exec, -1
	s_nop 1
	v_log_f32_e32 v18, v220
	v_log_f32_e32 v19, v221
	v_log_f32_e32 v20, v222
	v_log_f32_e32 v21, v223
	s_waitcnt lgkmcnt(0)
	v_pk_fma_f32 v[0:1], v[18:19], v[236:237], v[0:1]
	v_pk_fma_f32 v[0:1], v[20:21], v[238:239], v[0:1]
	ds_read_b128 v[236:239], v202 offset:80
	v_exp_f32_e64 v22, -v22
	v_exp_f32_e64 v23, -v23
	v_exp_f32_e64 v24, -v24
	v_exp_f32_e64 v25, -v25
	v_add_co_u32_e64 v200, s[42:43], v200, v200
	v_add_co_u32_e64 v200, s[48:49], v200, v200
	v_add_co_u32_e64 v200, s[50:51], v200, v200
	v_add_co_u32_e64 v200, s[56:57], v200, v200
	v_pk_add_f32 v[22:23], v[22:23], v[182:183]
	v_pk_add_f32 v[24:25], v[24:25], v[184:185]
	s_mov_b64 exec, s[42:43]
	v_mul_f32_e32 v224, v224, v22
	s_mov_b64 exec, s[48:49]
	v_mul_f32_e32 v225, v225, v23
	s_mov_b64 exec, s[50:51]
	v_mul_f32_e32 v226, v226, v24
	s_mov_b64 exec, s[56:57]
	v_mul_f32_e32 v227, v227, v25
	s_mov_b64 exec, -1
	s_nop 1
	v_log_f32_e32 v22, v224
	v_log_f32_e32 v23, v225
	v_log_f32_e32 v24, v226
	v_log_f32_e32 v25, v227
	s_waitcnt lgkmcnt(0)
	v_pk_fma_f32 v[0:1], v[22:23], v[236:237], v[0:1]
	v_pk_fma_f32 v[0:1], v[24:25], v[238:239], v[0:1]
	ds_read_b128 v[236:239], v202 offset:96
	v_exp_f32_e64 v26, -v26
	v_exp_f32_e64 v27, -v27
	v_exp_f32_e64 v28, -v28
	v_exp_f32_e64 v29, -v29
	v_add_co_u32_e64 v200, s[42:43], v200, v200
	v_add_co_u32_e64 v200, s[48:49], v200, v200
	v_add_co_u32_e64 v200, s[50:51], v200, v200
	v_add_co_u32_e64 v200, s[56:57], v200, v200
	v_pk_add_f32 v[26:27], v[26:27], v[186:187]
	v_pk_add_f32 v[28:29], v[28:29], v[188:189]
	s_mov_b64 exec, s[42:43]
	v_mul_f32_e32 v228, v228, v26
	s_mov_b64 exec, s[48:49]
	v_mul_f32_e32 v229, v229, v27
	s_mov_b64 exec, s[50:51]
	v_mul_f32_e32 v230, v230, v28
	s_mov_b64 exec, s[56:57]
	v_mul_f32_e32 v231, v231, v29
	s_mov_b64 exec, -1
	s_nop 1
	v_log_f32_e32 v26, v228
	v_log_f32_e32 v27, v229
	v_log_f32_e32 v28, v230
	v_log_f32_e32 v29, v231
	s_waitcnt lgkmcnt(0)
	v_pk_fma_f32 v[0:1], v[26:27], v[236:237], v[0:1]
	v_pk_fma_f32 v[0:1], v[28:29], v[238:239], v[0:1]
	ds_read_b128 v[236:239], v202 offset:112
	v_exp_f32_e64 v30, -v30
	v_exp_f32_e64 v31, -v31
	v_exp_f32_e64 v32, -v32
	v_exp_f32_e64 v33, -v33
	v_add_co_u32_e64 v200, s[42:43], v200, v200
	v_add_co_u32_e64 v200, s[48:49], v200, v200
	v_add_co_u32_e64 v200, s[50:51], v200, v200
	v_add_co_u32_e64 v200, s[56:57], v200, v200
	v_pk_add_f32 v[30:31], v[30:31], v[190:191]
	v_pk_add_f32 v[32:33], v[32:33], v[192:193]
	s_mov_b64 exec, s[42:43]
	v_mul_f32_e32 v232, v232, v30
	s_mov_b64 exec, s[48:49]
	v_mul_f32_e32 v233, v233, v31
	s_mov_b64 exec, s[50:51]
	v_mul_f32_e32 v234, v234, v32
	s_mov_b64 exec, s[56:57]
	v_mul_f32_e32 v235, v235, v33
	s_mov_b64 exec, -1
	s_nop 1
	v_log_f32_e32 v30, v232
	v_log_f32_e32 v31, v233
	v_log_f32_e32 v32, v234
	v_log_f32_e32 v33, v235
	s_waitcnt lgkmcnt(0)
	v_pk_fma_f32 v[0:1], v[30:31], v[236:237], v[0:1]
	v_pk_fma_f32 v[0:1], v[32:33], v[238:239], v[0:1]
.Lq2_halfdone:
	s_add_i32 s39, s39, 1
	s_cmp_lt_u32 s39, 4
	s_cbranch_scc1 .Lq2_loop
	v_add_f32_e32 v201, v0, v1
